# k_bhist weight-packing blocks: coalesced prefetch of all weight arrays into the XCD's L2 before the serialized packing loops
# baseline (speedup 1.0000x reference)
.LBB2_20:
	s_and_b64 vcc, exec, s[4:5]
	s_cbranch_vccz .LBB2_66
	s_load_dwordx4 s[20:23], s[0:1], 0x18
	s_load_dwordx4 s[24:27], s[0:1], 0x30
	s_load_dwordx2 s[28:29], s[0:1], 0x40
	s_load_dwordx2 s[30:31], s[0:1], 0x58
	s_lshr_b32 s19, s2, 3
	s_and_b32 s19, s19, 7
	s_lshl_b32 s19, s19, 10
	v_or_b32_e32 v32, s19, v0
	v_lshlrev_b32_e32 v33, 4, v32
	s_waitcnt lgkmcnt(0)
	v_cmp_gt_u32_e32 vcc, 0x400, v32
	s_and_saveexec_b64 s[32:33], vcc
	global_load_dwordx4 v[36:39], v33, s[20:21]
	s_mov_b64 exec, s[32:33]
	v_cmp_gt_u32_e32 vcc, 0x1000, v32
	s_and_saveexec_b64 s[32:33], vcc
	global_load_dwordx4 v[36:39], v33, s[22:23]
	s_mov_b64 exec, s[32:33]
	global_load_dwordx4 v[36:39], v33, s[24:25]
	s_add_u32 s34, s24, 0x20000
	s_addc_u32 s35, s25, 0
	global_load_dwordx4 v[36:39], v33, s[34:35]
	global_load_dwordx4 v[36:39], v33, s[26:27]
	s_add_u32 s34, s26, 0x20000
	s_addc_u32 s35, s27, 0
	global_load_dwordx4 v[36:39], v33, s[34:35]
	global_load_dwordx4 v[36:39], v33, s[28:29]
	s_add_u32 s34, s28, 0x20000
	s_addc_u32 s35, s29, 0
	global_load_dwordx4 v[36:39], v33, s[34:35]
	global_load_dwordx4 v[36:39], v33, s[30:31]
	s_add_u32 s34, s30, 0x20000
	s_addc_u32 s35, s31, 0
	global_load_dwordx4 v[36:39], v33, s[34:35]
	s_add_u32 s34, s30, 0x40000
	s_addc_u32 s35, s31, 0
	global_load_dwordx4 v[36:39], v33, s[34:35]
	s_lshl_b32 s16, s2, 10
	s_add_i32 s2, s16, 0xfffc0000
	v_or_b32_e32 v2, s2, v0
	s_movk_i32 s2, 0x1000
	v_cmp_gt_i32_e32 vcc, s2, v2
	v_or_b32_e32 v5, s16, v0
	v_and_b32_e32 v4, 7, v0
	s_and_saveexec_b64 s[2:3], vcc
	s_cbranch_execz .LBB2_29
	s_load_dwordx2 s[6:7], s[0:1], 0x60
	s_load_dwordx2 s[4:5], s[0:1], 0x18
	v_max_i32_e32 v1, 0xffff1000, v2
	v_sub_u32_e32 v1, v1, v5
	v_add_u32_e32 v1, 0x4ffff, v1
	s_mov_b32 s8, 0xffff
	v_cmp_lt_u32_e32 vcc, s8, v1
	s_mov_b64 s[10:11], -1
	v_mov_b32_e32 v6, v2
	s_and_saveexec_b64 s[8:9], vcc
	s_cbranch_execz .LBB2_26
	v_mov_b32_e32 v3, 1
	v_add_u32_sdwa v8, v1, v3 dst_sel:DWORD dst_unused:UNUSED_PAD src0_sel:WORD_1 src1_sel:DWORD
	v_and_b32_e32 v9, 0x1fffe, v8
	v_add_u32_e32 v3, 0x10000, v2
	v_mov_b32_e32 v1, v4
	s_mov_b64 s[10:11], 0
	v_mov_b32_e32 v10, v9
	v_mov_b64_e32 v[6:7], v[2:3]

	.amdhsa_kernel _Z7k_bhistPKiPiPfPKfS4_PDF16_S4_S4_S4_S4_S4_S4_S5_S5_S5_S5_S2_
		.amdhsa_group_segment_fixed_size 628
		.amdhsa_private_segment_fixed_size 0
		.amdhsa_kernarg_size 136
		.amdhsa_user_sgpr_count 2
		.amdhsa_user_sgpr_dispatch_ptr 0
		.amdhsa_user_sgpr_queue_ptr 0
		.amdhsa_user_sgpr_kernarg_segment_ptr 1
		.amdhsa_user_sgpr_dispatch_id 0
		.amdhsa_user_sgpr_kernarg_preload_length 0
		.amdhsa_user_sgpr_kernarg_preload_offset 0
		.amdhsa_user_sgpr_private_segment_size 0
		.amdhsa_uses_dynamic_stack 0
		.amdhsa_enable_private_segment 0
		.amdhsa_system_sgpr_workgroup_id_x 1
		.amdhsa_system_sgpr_workgroup_id_y 0
		.amdhsa_system_sgpr_workgroup_id_z 0
		.amdhsa_system_sgpr_workgroup_info 0
		.amdhsa_system_vgpr_workitem_id 0
		.amdhsa_next_free_vgpr 40
		.amdhsa_next_free_sgpr 36
		.amdhsa_accum_offset 40
		.amdhsa_reserve_vcc 1
		.amdhsa_float_round_mode_32 0
		.amdhsa_float_round_mode_16_64 0
		.amdhsa_float_denorm_mode_32 3
		.amdhsa_float_denorm_mode_16_64 3
		.amdhsa_dx10_clamp 1
		.amdhsa_ieee_mode 1
		.amdhsa_fp16_overflow 0
		.amdhsa_tg_split 0
		.amdhsa_exception_fp_ieee_invalid_op 0
		.amdhsa_exception_fp_denorm_src 0
		.amdhsa_exception_fp_ieee_div_zero 0
		.amdhsa_exception_fp_ieee_overflow 0
		.amdhsa_exception_fp_ieee_underflow 0
		.amdhsa_exception_fp_ieee_inexact 0
		.amdhsa_exception_int_div_zero 0
	.end_amdhsa_kernel

amdhsa.kernels:
  - .agpr_count:     0
    .args:
      - .actual_access:  read_only
        .address_space:  global
        .offset:         0
        .size:           8
        .value_kind:     global_buffer
      - .actual_access:  read_only
        .address_space:  global
        .offset:         8
        .size:           8
        .value_kind:     global_buffer
      - .actual_access:  read_only
        .address_space:  global
        .offset:         16
        .size:           8
        .value_kind:     global_buffer
      - .actual_access:  read_only
        .address_space:  global
        .offset:         24
        .size:           8
        .value_kind:     global_buffer
      - .actual_access:  write_only
        .address_space:  global
        .offset:         32
        .size:           8
        .value_kind:     global_buffer
      - .actual_access:  write_only
        .address_space:  global
        .offset:         40
        .size:           8
        .value_kind:     global_buffer
    .group_segment_fixed_size: 56512
    .kernarg_segment_align: 8
    .kernarg_segment_size: 48
    .language:       OpenCL C
    .language_version:
      - 2
      - 0
    .max_flat_workgroup_size: 1024
    .name:           _Z10k_bscatterPKiS0_PKfS0_PiP15HIP_vector_typeIiLj2EE
    .private_segment_fixed_size: 0
    .sgpr_count:     42
    .sgpr_spill_count: 0
    .symbol:         _Z10k_bscatterPKiS0_PKfS0_PiP15HIP_vector_typeIiLj2EE.kd
    .uniform_work_group_size: 1
    .uses_dynamic_stack: false
    .vgpr_count:     89
    .vgpr_spill_count: 0
    .wavefront_size: 64
  - .agpr_count:     0
    .args:
      - .actual_access:  read_only
        .address_space:  global
        .offset:         0
        .size:           8
        .value_kind:     global_buffer
      - .actual_access:  read_only
        .address_space:  global
        .offset:         8
        .size:           8
        .value_kind:     global_buffer
      - .actual_access:  write_only
        .address_space:  global
        .offset:         16
        .size:           8
        .value_kind:     global_buffer
      - .actual_access:  write_only
        .address_space:  global
        .offset:         24
        .size:           8
        .value_kind:     global_buffer
      - .actual_access:  write_only
        .address_space:  global
        .offset:         32
        .size:           8
        .value_kind:     global_buffer
      - .actual_access:  write_only
        .address_space:  global
        .offset:         40
        .size:           8
        .value_kind:     global_buffer
      - .actual_access:  read_only
        .address_space:  global
        .offset:         48
        .size:           8
        .value_kind:     global_buffer
      - .actual_access:  write_only
        .address_space:  global
        .offset:         56
        .size:           8
        .value_kind:     global_buffer
    .group_segment_fixed_size: 12352
    .kernarg_segment_align: 8
    .kernarg_segment_size: 64
    .language:       OpenCL C
    .language_version:
      - 2
      - 0
    .max_flat_workgroup_size: 1024
    .name:           _Z8k_bfinalPK15HIP_vector_typeIiLj2EEPKiPS0_PiS6_PfPKfPDF16_
    .private_segment_fixed_size: 0
    .sgpr_count:     38
    .sgpr_spill_count: 0
    .symbol:         _Z8k_bfinalPK15HIP_vector_typeIiLj2EEPKiPS0_PiS6_PfPKfPDF16_.kd
    .uniform_work_group_size: 1
    .uses_dynamic_stack: false
    .vgpr_count:     72
    .vgpr_spill_count: 0
    .wavefront_size: 64
  - .agpr_count:     0
    .args:
      - .actual_access:  read_only
        .address_space:  global
        .offset:         0
        .size:           8
        .value_kind:     global_buffer
      - .actual_access:  write_only
        .address_space:  global
        .offset:         8
        .size:           8
        .value_kind:     global_buffer
      - .actual_access:  write_only
        .address_space:  global
        .offset:         16
        .size:           8
        .value_kind:     global_buffer
      - .actual_access:  read_only
        .address_space:  global
        .offset:         24
        .size:           8
        .value_kind:     global_buffer
      - .actual_access:  read_only
        .address_space:  global
        .offset:         32
        .size:           8
        .value_kind:     global_buffer
      - .actual_access:  write_only
        .address_space:  global
        .offset:         40
        .size:           8
        .value_kind:     global_buffer
      - .actual_access:  read_only
        .address_space:  global
        .offset:         48
        .size:           8
        .value_kind:     global_buffer
      - .actual_access:  read_only
        .address_space:  global
        .offset:         56
        .size:           8
        .value_kind:     global_buffer
      - .actual_access:  read_only
        .address_space:  global
        .offset:         64
        .size:           8
        .value_kind:     global_buffer
      - .actual_access:  read_only
        .address_space:  global
        .offset:         72
        .size:           8
        .value_kind:     global_buffer
      - .actual_access:  read_only
        .address_space:  global
        .offset:         80
        .size:           8
        .value_kind:     global_buffer
      - .actual_access:  read_only
        .address_space:  global
        .offset:         88
        .size:           8
        .value_kind:     global_buffer
      - .actual_access:  write_only
        .address_space:  global
        .offset:         96
        .size:           8
        .value_kind:     global_buffer
      - .actual_access:  write_only
        .address_space:  global
        .offset:         104
        .size:           8
        .value_kind:     global_buffer
      - .actual_access:  write_only
        .address_space:  global
        .offset:         112
        .size:           8
        .value_kind:     global_buffer
      - .actual_access:  write_only
        .address_space:  global
        .offset:         120
        .size:           8
        .value_kind:     global_buffer
      - .actual_access:  write_only
        .address_space:  global
        .offset:         128
        .size:           8
        .value_kind:     global_buffer
    .group_segment_fixed_size: 628
    .kernarg_segment_align: 8
    .kernarg_segment_size: 136
    .language:       OpenCL C
    .language_version:
      - 2
      - 0
    .max_flat_workgroup_size: 1024
    .name:           _Z7k_bhistPKiPiPfPKfS4_PDF16_S4_S4_S4_S4_S4_S4_S5_S5_S5_S5_S2_
    .private_segment_fixed_size: 0
    .sgpr_count:     42
    .sgpr_spill_count: 0
    .symbol:         _Z7k_bhistPKiPiPfPKfS4_PDF16_S4_S4_S4_S4_S4_S4_S5_S5_S5_S5_S2_.kd
    .uniform_work_group_size: 1
    .uses_dynamic_stack: false
    .vgpr_count:     40
    .vgpr_spill_count: 0
    .wavefront_size: 64
  - .agpr_count:     0
    .args:
      - .actual_access:  read_only
        .address_space:  global
        .offset:         0
        .size:           8
        .value_kind:     global_buffer
      - .actual_access:  read_only
        .address_space:  global
        .offset:         8
        .size:           8
        .value_kind:     global_buffer
      - .actual_access:  read_only
        .address_space:  global
        .offset:         16
        .size:           8
        .value_kind:     global_buffer
      - .actual_access:  read_only
        .address_space:  global
        .offset:         24
        .size:           8
        .value_kind:     global_buffer
      - .actual_access:  read_only
        .address_space:  global
        .offset:         32
        .size:           8
        .value_kind:     global_buffer
      - .actual_access:  read_only
        .address_space:  global
        .offset:         40
        .size:           8
        .value_kind:     global_buffer
      - .actual_access:  read_only
        .address_space:  global
        .offset:         48
        .size:           8
        .value_kind:     global_buffer
      - .actual_access:  read_only
        .address_space:  global
        .offset:         56
        .size:           8
        .value_kind:     global_buffer
      - .actual_access:  read_only
        .address_space:  global
        .offset:         64
        .size:           8
        .value_kind:     global_buffer
      - .actual_access:  write_only
        .address_space:  global
        .offset:         72
        .size:           8
        .value_kind:     global_buffer
      - .actual_access:  write_only
        .address_space:  global
        .offset:         80
        .size:           8
        .value_kind:     global_buffer
      - .offset:         88
        .size:           4
        .value_kind:     hidden_block_count_x
      - .offset:         92
        .size:           4
        .value_kind:     hidden_block_count_y
      - .offset:         96
        .size:           4
        .value_kind:     hidden_block_count_z
      - .offset:         100
        .size:           2
        .value_kind:     hidden_group_size_x
      - .offset:         102
        .size:           2
        .value_kind:     hidden_group_size_y
      - .offset:         104
        .size:           2
        .value_kind:     hidden_group_size_z
      - .offset:         106
        .size:           2
        .value_kind:     hidden_remainder_x
      - .offset:         108
        .size:           2
        .value_kind:     hidden_remainder_y
      - .offset:         110
        .size:           2
        .value_kind:     hidden_remainder_z
      - .offset:         128
        .size:           8
        .value_kind:     hidden_global_offset_x
      - .offset:         136
        .size:           8
        .value_kind:     hidden_global_offset_y
      - .offset:         144
        .size:           8
        .value_kind:     hidden_global_offset_z
      - .offset:         152
        .size:           2
        .value_kind:     hidden_grid_dims
    .group_segment_fixed_size: 2048
    .kernarg_segment_align: 8
    .kernarg_segment_size: 344
    .language:       OpenCL C
    .language_version:
      - 2
      - 0
    .max_flat_workgroup_size: 256
    .name:           _Z7k_fold2PKfS0_S0_S0_S0_S0_S0_S0_S0_PDF16_Pf
    .private_segment_fixed_size: 0
    .sgpr_count:     44
    .sgpr_spill_count: 0
    .symbol:         _Z7k_fold2PKfS0_S0_S0_S0_S0_S0_S0_S0_PDF16_Pf.kd
    .uniform_work_group_size: 1
    .uses_dynamic_stack: false
    .vgpr_count:     61
    .vgpr_spill_count: 0
    .wavefront_size: 64
  - .agpr_count:     0
    .args:
      - .actual_access:  read_only
        .address_space:  global
        .offset:         0
        .size:           8
        .value_kind:     global_buffer
      - .actual_access:  read_only
        .address_space:  global
        .offset:         8
        .size:           8
        .value_kind:     global_buffer
      - .actual_access:  write_only
        .address_space:  global
        .offset:         16
        .size:           8
        .value_kind:     global_buffer
      - .actual_access:  read_only
        .address_space:  global
        .offset:         24
        .size:           8
        .value_kind:     global_buffer
      - .actual_access:  read_only
        .address_space:  global
        .offset:         32
        .size:           8
        .value_kind:     global_buffer
      - .actual_access:  read_only
        .address_space:  global
        .offset:         40
        .size:           8
        .value_kind:     global_buffer
      - .actual_access:  read_only
        .address_space:  global
        .offset:         48
        .size:           8
        .value_kind:     global_buffer
      - .actual_access:  read_only
        .address_space:  global
        .offset:         56
        .size:           8
        .value_kind:     global_buffer
      - .actual_access:  read_only
        .address_space:  global
        .offset:         64
        .size:           8
        .value_kind:     global_buffer
      - .actual_access:  read_only
        .address_space:  global
        .offset:         72
        .size:           8
        .value_kind:     global_buffer
      - .actual_access:  read_only
        .address_space:  global
        .offset:         80
        .size:           8
        .value_kind:     global_buffer
      - .actual_access:  write_only
        .address_space:  global
        .offset:         88
        .size:           8
        .value_kind:     global_buffer
      - .actual_access:  write_only
        .address_space:  global
        .offset:         96
        .size:           8
        .value_kind:     global_buffer
      - .address_space:  global
        .offset:         104
        .size:           8
        .value_kind:     global_buffer
      - .actual_access:  write_only
        .address_space:  global
        .offset:         112
        .size:           8
        .value_kind:     global_buffer
      - .actual_access:  read_only
        .address_space:  global
        .offset:         120
        .size:           8
        .value_kind:     global_buffer
      - .actual_access:  read_only
        .address_space:  global
        .offset:         128
        .size:           8
        .value_kind:     global_buffer
    .group_segment_fixed_size: 22272
    .kernarg_segment_align: 8
    .kernarg_segment_size: 136
    .language:       OpenCL C
    .language_version:
      - 2
      - 0
    .max_flat_workgroup_size: 256
    .name:           _Z5k_gcnILi1EEvPKvPK15HIP_vector_typeIiLj2EEPfPKiS8_PKfPKDF16_SA_SA_SA_SA_S6_PDF16_S6_SD_SC_SA_
    .private_segment_fixed_size: 0
    .sgpr_count:     35
    .sgpr_spill_count: 0
    .symbol:         _Z5k_gcnILi1EEvPKvPK15HIP_vector_typeIiLj2EEPfPKiS8_PKfPKDF16_SA_SA_SA_SA_S6_PDF16_S6_SD_SC_SA_.kd
    .uniform_work_group_size: 1
    .uses_dynamic_stack: false
    .vgpr_count:     72
    .vgpr_spill_count: 0
    .wavefront_size: 64
  - .agpr_count:     0
    .args:
      - .actual_access:  read_only
        .address_space:  global
        .offset:         0
        .size:           8
        .value_kind:     global_buffer
      - .actual_access:  read_only
        .address_space:  global
        .offset:         8
        .size:           8
        .value_kind:     global_buffer
      - .actual_access:  read_only
        .address_space:  global
        .offset:         16
        .size:           8
        .value_kind:     global_buffer
      - .actual_access:  read_only
        .address_space:  global
        .offset:         24
        .size:           8
        .value_kind:     global_buffer
      - .actual_access:  read_only
        .address_space:  global
        .offset:         32
        .size:           8
        .value_kind:     global_buffer
      - .actual_access:  read_only
        .address_space:  global
        .offset:         40
        .size:           8
        .value_kind:     global_buffer
      - .actual_access:  read_only
        .address_space:  global
        .offset:         48
        .size:           8
        .value_kind:     global_buffer
      - .actual_access:  read_only
        .address_space:  global
        .offset:         56
        .size:           8
        .value_kind:     global_buffer
      - .actual_access:  read_only
        .address_space:  global
        .offset:         64
        .size:           8
        .value_kind:     global_buffer
      - .actual_access:  read_only
        .address_space:  global
        .offset:         72
        .size:           8
        .value_kind:     global_buffer
      - .actual_access:  read_only
        .address_space:  global
        .offset:         80
        .size:           8
        .value_kind:     global_buffer
      - .actual_access:  read_only
        .address_space:  global
        .offset:         88
        .size:           8
        .value_kind:     global_buffer
      - .actual_access:  write_only
        .address_space:  global
        .offset:         96
        .size:           8
        .value_kind:     global_buffer
      - .address_space:  global
        .offset:         104
        .size:           8
        .value_kind:     global_buffer
      - .actual_access:  read_only
        .address_space:  global
        .offset:         112
        .size:           8
        .value_kind:     global_buffer
      - .actual_access:  read_only
        .address_space:  global
        .offset:         120
        .size:           8
        .value_kind:     global_buffer
      - .actual_access:  read_only
        .address_space:  global
        .offset:         128
        .size:           8
        .value_kind:     global_buffer
      - .offset:         136
        .size:           4
        .value_kind:     hidden_block_count_x
      - .offset:         140
        .size:           4
        .value_kind:     hidden_block_count_y
      - .offset:         144
        .size:           4
        .value_kind:     hidden_block_count_z
      - .offset:         148
        .size:           2
        .value_kind:     hidden_group_size_x
      - .offset:         150
        .size:           2
        .value_kind:     hidden_group_size_y
      - .offset:         152
        .size:           2
        .value_kind:     hidden_group_size_z
      - .offset:         154
        .size:           2
        .value_kind:     hidden_remainder_x
      - .offset:         156
        .size:           2
        .value_kind:     hidden_remainder_y
      - .offset:         158
        .size:           2
        .value_kind:     hidden_remainder_z
      - .offset:         176
        .size:           8
        .value_kind:     hidden_global_offset_x
      - .offset:         184
        .size:           8
        .value_kind:     hidden_global_offset_y
      - .offset:         192
        .size:           8
        .value_kind:     hidden_global_offset_z
      - .offset:         200
        .size:           2
        .value_kind:     hidden_grid_dims
    .group_segment_fixed_size: 32000
    .kernarg_segment_align: 8
    .kernarg_segment_size: 392
    .language:       OpenCL C
    .language_version:
      - 2
      - 0
    .max_flat_workgroup_size: 256
    .name:           _Z5k_gcnILi2EEvPKvPK15HIP_vector_typeIiLj2EEPfPKiS8_PKfPKDF16_SA_SA_SA_SA_S6_PDF16_S6_SD_SC_SA_
    .private_segment_fixed_size: 0
    .sgpr_count:     36
    .sgpr_spill_count: 0
    .symbol:         _Z5k_gcnILi2EEvPKvPK15HIP_vector_typeIiLj2EEPfPKiS8_PKfPKDF16_SA_SA_SA_SA_S6_PDF16_S6_SD_SC_SA_.kd
    .uniform_work_group_size: 1
    .uses_dynamic_stack: false
    .vgpr_count:     128
    .vgpr_spill_count: 0
    .wavefront_size: 64
  - .agpr_count:     0
    .args:
      - .actual_access:  read_only
        .address_space:  global
        .offset:         0
        .size:           8
        .value_kind:     global_buffer
      - .actual_access:  read_only
        .address_space:  global
        .offset:         8
        .size:           8
        .value_kind:     global_buffer
      - .actual_access:  read_only
        .address_space:  global
        .offset:         16
        .size:           8
        .value_kind:     global_buffer
      - .actual_access:  read_only
        .address_space:  global
        .offset:         24
        .size:           8
        .value_kind:     global_buffer
      - .actual_access:  write_only
        .address_space:  global
        .offset:         32
        .size:           8
        .value_kind:     global_buffer
      - .actual_access:  read_only
        .address_space:  global
        .offset:         40
        .size:           8
        .value_kind:     global_buffer
      - .actual_access:  read_only
        .address_space:  global
        .offset:         48
        .size:           8
        .value_kind:     global_buffer
      - .actual_access:  read_only
        .address_space:  global
        .offset:         56
        .size:           8
        .value_kind:     global_buffer
      - .actual_access:  read_only
        .address_space:  global
        .offset:         64
        .size:           8
        .value_kind:     global_buffer
      - .actual_access:  read_only
        .address_space:  global
        .offset:         72
        .size:           8
        .value_kind:     global_buffer
      - .actual_access:  read_only
        .address_space:  global
        .offset:         80
        .size:           8
        .value_kind:     global_buffer
      - .actual_access:  read_only
        .address_space:  global
        .offset:         88
        .size:           8
        .value_kind:     global_buffer
      - .actual_access:  write_only
        .address_space:  global
        .offset:         96
        .size:           8
        .value_kind:     global_buffer
    .group_segment_fixed_size: 9216
    .kernarg_segment_align: 8
    .kernarg_segment_size: 104
    .language:       OpenCL C
    .language_version:
      - 2
      - 0
    .max_flat_workgroup_size: 512
    .name:           _Z6k_lstmILi256ELi10ELb1ELb0EEvPKDF16_S1_S1_PKfPDF16_S1_S1_S1_S3_S3_S3_PfS5_
    .private_segment_fixed_size: 0
    .sgpr_count:     37
    .sgpr_spill_count: 0
    .symbol:         _Z6k_lstmILi256ELi10ELb1ELb0EEvPKDF16_S1_S1_PKfPDF16_S1_S1_S1_S3_S3_S3_PfS5_.kd
    .uniform_work_group_size: 1
    .uses_dynamic_stack: false
    .vgpr_count:     256
    .vgpr_spill_count: 0
    .wavefront_size: 64
  - .agpr_count:     0
    .args:
      - .actual_access:  read_only
        .address_space:  global
        .offset:         0
        .size:           8
        .value_kind:     global_buffer
      - .actual_access:  read_only
        .address_space:  global
        .offset:         8
        .size:           8
        .value_kind:     global_buffer
      - .actual_access:  read_only
        .address_space:  global
        .offset:         16
        .size:           8
        .value_kind:     global_buffer
      - .actual_access:  read_only
        .address_space:  global
        .offset:         24
        .size:           8
        .value_kind:     global_buffer
      - .actual_access:  read_only
        .address_space:  global
        .offset:         32
        .size:           8
        .value_kind:     global_buffer
      - .actual_access:  read_only
        .address_space:  global
        .offset:         40
        .size:           8
        .value_kind:     global_buffer
      - .actual_access:  read_only
        .address_space:  global
        .offset:         48
        .size:           8
        .value_kind:     global_buffer
      - .actual_access:  read_only
        .address_space:  global
        .offset:         56
        .size:           8
        .value_kind:     global_buffer
      - .actual_access:  read_only
        .address_space:  global
        .offset:         64
        .size:           8
        .value_kind:     global_buffer
      - .actual_access:  read_only
        .address_space:  global
        .offset:         72
        .size:           8
        .value_kind:     global_buffer
      - .actual_access:  read_only
        .address_space:  global
        .offset:         80
        .size:           8
        .value_kind:     global_buffer
      - .actual_access:  write_only
        .address_space:  global
        .offset:         88
        .size:           8
        .value_kind:     global_buffer
      - .actual_access:  read_only
        .address_space:  global
        .offset:         96
        .size:           8
        .value_kind:     global_buffer
    .group_segment_fixed_size: 0
    .kernarg_segment_align: 8
    .kernarg_segment_size: 104
    .language:       OpenCL C
    .language_version:
      - 2
      - 0
    .max_flat_workgroup_size: 512
    .name:           _Z6k_lstmILi128ELi8ELb0ELb1EEvPKDF16_S1_S1_PKfPDF16_S1_S1_S1_S3_S3_S3_PfS5_
    .private_segment_fixed_size: 0
    .sgpr_count:     46
    .sgpr_spill_count: 0
    .symbol:         _Z6k_lstmILi128ELi8ELb0ELb1EEvPKDF16_S1_S1_PKfPDF16_S1_S1_S1_S3_S3_S3_PfS5_.kd
    .uniform_work_group_size: 1
    .uses_dynamic_stack: false
    .vgpr_count:     256
    .vgpr_spill_count: 0
    .wavefront_size: 64
